# v23: v22 + out-projection epilogue loads both halves' gate vectors up front (second exposed load latency and store drain removed)
# speedup vs baseline: 1.0111x; 1.0040x over previous
.Lpeel_exit_2:
	s_ashr_i32 s2, s13, 4
	s_mul_hi_i32 s3, s2, 0xc000
	s_mul_i32 s2, s2, 0xc000
	s_add_u32 s7, s69, s2
	s_addc_u32 s20, s71, s3
	s_lshl_b32 s2, s15, 8
	s_ashr_i32 s3, s2, 31
	s_lshl_b64 s[24:25], s[2:3], 2
	s_add_u32 s7, s7, s24
	v_mbcnt_lo_u32_b32 v132, -1, 0
	v_mbcnt_hi_u32_b32 v132, -1, v132
	s_addc_u32 s15, s20, s25
	v_ashrrev_i32_e32 v136, 4, v132
	s_lshl_b32 s20, s23, 2
	s_add_u32 s24, s7, s20
	v_lshlrev_b32_e32 v128, 2, v136
	s_addc_u32 s25, s15, 0
	v_ashrrev_i32_e32 v129, 31, v128
	v_lshl_add_u64 v[130:131], v[128:129], 2, s[24:25]
	v_lshlrev_b32_e32 v128, 3, v136
	global_load_dwordx4 v[136:139], v[130:131], off
	global_load_dwordx4 v[152:155], v[130:131], off offset:64
	global_load_dwordx4 v[196:199], v[130:131], off offset:512
	global_load_dwordx4 v[200:203], v[130:131], off offset:576
	s_lshl_b32 s7, s13, 8
	s_add_i32 s24, s7, s16
	s_ashr_i32 s25, s24, 31
	s_lshl_b64 s[24:25], s[24:25], 11
	s_add_u32 s7, s61, s24
	s_addc_u32 s13, s65, s25
	s_add_u32 s2, s7, s2
	s_addc_u32 s3, s13, s3
	v_bfi_b32 v128, -16, v128, v132
	s_add_u32 s2, s2, s23
	v_ashrrev_i32_e32 v129, 31, v128
	s_addc_u32 s3, s3, 0
	v_lshlrev_b64 v[128:129], 11, v[128:129]
	v_lshl_add_u64 v[128:129], s[2:3], 0, v[128:129]
	v_and_b32_e32 v132, 16, v132
	v_lshl_add_u64 v[128:129], v[128:129], 0, v[132:133]
	s_mov_b32 s2, 0x10000
	s_mov_b32 s13, s36
	s_mov_b32 s15, s6
	s_mov_b64 s[34:35], s[58:59]
	s_waitcnt vmcnt(0)
	v_pk_mul_f32 v[140:141], v[138:139], s[54:55] op_sel_hi:[1,0]
	v_pk_mul_f32 v[138:139], v[136:137], s[54:55] op_sel_hi:[1,0]
	v_pk_mul_f32 v[136:137], v[152:153], s[54:55] op_sel_hi:[1,0]
	v_pk_mul_f32 v[152:153], v[124:125], v[138:139]
	v_mov_b32_e32 v124, v133
	v_cvt_pk_fp8_f32 v124, v152, v153
	v_pk_mul_f32 v[126:127], v[126:127], v[140:141]
	v_pk_mul_f32 v[112:113], v[112:113], v[136:137]
	v_pk_mul_f32 v[110:111], v[110:111], v[140:141]
	v_cvt_pk_fp8_f32 v124, v126, v127 op_sel:[0,0,1]
	v_mov_b32_e32 v127, v133
	v_cvt_pk_fp8_f32 v127, v112, v113
	v_pk_mul_f32 v[112:113], v[108:109], v[138:139]
	v_mov_b32_e32 v108, v133
	v_cvt_pk_fp8_f32 v108, v112, v113
	v_pk_mul_f32 v[96:97], v[96:97], v[136:137]
	v_pk_mul_f32 v[142:143], v[154:155], s[54:55] op_sel_hi:[1,0]
	v_pk_mul_f32 v[94:95], v[94:95], v[140:141]
	v_cvt_pk_fp8_f32 v108, v110, v111 op_sel:[0,0,1]
	v_mov_b32_e32 v111, v133
	v_cvt_pk_fp8_f32 v111, v96, v97
	v_pk_mul_f32 v[98:99], v[98:99], v[142:143]
	v_pk_mul_f32 v[80:81], v[80:81], v[136:137]
	v_pk_mul_f32 v[78:79], v[78:79], v[140:141]
	v_cvt_pk_fp8_f32 v111, v98, v99 op_sel:[0,0,1]
	v_pk_mul_f32 v[98:99], v[92:93], v[138:139]
	v_mov_b32_e32 v92, v133
	v_cvt_pk_fp8_f32 v92, v98, v99
	v_pk_mul_f32 v[120:121], v[120:121], v[136:137]
	v_mov_b32_e32 v125, v133
	v_pk_mul_f32 v[116:117], v[116:117], v[138:139]
	v_cvt_pk_fp8_f32 v92, v94, v95 op_sel:[0,0,1]
	v_mov_b32_e32 v95, v133
	v_cvt_pk_fp8_f32 v95, v80, v81
	v_pk_mul_f32 v[80:81], v[76:77], v[138:139]
	v_mov_b32_e32 v76, v133
	v_cvt_pk_fp8_f32 v76, v80, v81
	v_mov_b32_e32 v126, v133
	v_pk_mul_f32 v[104:105], v[104:105], v[136:137]
	v_mov_b32_e32 v109, v133
	v_pk_mul_f32 v[100:101], v[100:101], v[138:139]
	v_mov_b32_e32 v110, v133
	v_pk_mul_f32 v[88:89], v[88:89], v[136:137]
	v_mov_b32_e32 v93, v133
	v_pk_mul_f32 v[84:85], v[84:85], v[138:139]
	v_mov_b32_e32 v94, v133
	v_cvt_pk_fp8_f32 v76, v78, v79 op_sel:[0,0,1]
	v_pk_mul_f32 v[72:73], v[72:73], v[136:137]
	v_mov_b32_e32 v77, v133
	v_pk_mul_f32 v[68:69], v[68:69], v[138:139]
	v_mov_b32_e32 v78, v133
	v_pk_mul_f32 v[64:65], v[64:65], v[136:137]
	v_mov_b32_e32 v79, v133
	v_cvt_pk_fp8_f32 v125, v120, v121
	v_cvt_pk_fp8_f32 v126, v116, v117
	v_cvt_pk_fp8_f32 v109, v104, v105
	v_cvt_pk_fp8_f32 v110, v100, v101
	v_cvt_pk_fp8_f32 v93, v88, v89
	v_cvt_pk_fp8_f32 v94, v84, v85
	v_cvt_pk_fp8_f32 v77, v72, v73
	v_cvt_pk_fp8_f32 v78, v68, v69
	v_cvt_pk_fp8_f32 v79, v64, v65
	v_pk_mul_f32 v[122:123], v[122:123], v[142:143]
	v_pk_mul_f32 v[118:119], v[118:119], v[140:141]
	v_pk_mul_f32 v[114:115], v[114:115], v[142:143]
	v_pk_mul_f32 v[106:107], v[106:107], v[142:143]
	v_pk_mul_f32 v[102:103], v[102:103], v[140:141]
	v_pk_mul_f32 v[90:91], v[90:91], v[142:143]
	v_pk_mul_f32 v[86:87], v[86:87], v[140:141]
	v_pk_mul_f32 v[82:83], v[82:83], v[142:143]
	v_pk_mul_f32 v[74:75], v[74:75], v[142:143]
	v_pk_mul_f32 v[70:71], v[70:71], v[140:141]
	v_pk_mul_f32 v[66:67], v[66:67], v[142:143]
	v_cvt_pk_fp8_f32 v125, v122, v123 op_sel:[0,0,1]
	v_cvt_pk_fp8_f32 v126, v118, v119 op_sel:[0,0,1]
	v_cvt_pk_fp8_f32 v127, v114, v115 op_sel:[0,0,1]
	v_cvt_pk_fp8_f32 v109, v106, v107 op_sel:[0,0,1]
	v_cvt_pk_fp8_f32 v110, v102, v103 op_sel:[0,0,1]
	v_add_co_u32_e32 v96, vcc, s2, v128
	v_cvt_pk_fp8_f32 v93, v90, v91 op_sel:[0,0,1]
	v_cvt_pk_fp8_f32 v94, v86, v87 op_sel:[0,0,1]
	v_cvt_pk_fp8_f32 v95, v82, v83 op_sel:[0,0,1]
	v_cvt_pk_fp8_f32 v77, v74, v75 op_sel:[0,0,1]
	v_cvt_pk_fp8_f32 v78, v70, v71 op_sel:[0,0,1]
	v_cvt_pk_fp8_f32 v79, v66, v67 op_sel:[0,0,1]
	v_addc_co_u32_e32 v97, vcc, 0, v129, vcc
	s_mov_b32 s2, 0x40000
	v_add_co_u32_e32 v64, vcc, s2, v128
	s_mov_b32 s2, 0x50000
	s_nop 0
	v_addc_co_u32_e32 v65, vcc, 0, v129, vcc
	v_permlane32_swap_b32_e32 v124, v126
	v_permlane32_swap_b32_e32 v125, v127
	v_permlane32_swap_b32_e32 v108, v110
	v_permlane32_swap_b32_e32 v109, v111
	v_permlane32_swap_b32_e32 v92, v94
	v_permlane32_swap_b32_e32 v93, v95
	v_permlane32_swap_b32_e32 v76, v78
	v_permlane32_swap_b32_e32 v77, v79
	v_add_co_u32_e32 v66, vcc, s2, v128
	v_permlane16_swap_b32_e32 v124, v125
	v_permlane16_swap_b32_e32 v126, v127
	v_permlane16_swap_b32_e32 v108, v109
	v_permlane16_swap_b32_e32 v110, v111
	v_permlane16_swap_b32_e32 v92, v93
	v_permlane16_swap_b32_e32 v94, v95
	v_permlane16_swap_b32_e32 v76, v77
	v_permlane16_swap_b32_e32 v78, v79
	v_addc_co_u32_e32 v67, vcc, 0, v129, vcc
	global_store_dwordx4 v[128:129], v[124:127], off
	global_store_dwordx4 v[96:97], v[108:111], off
	global_store_dwordx4 v[64:65], v[92:95], off
	global_store_dwordx4 v[66:67], v[76:79], off
	s_and_b64 vcc, exec, s[4:5]
	s_mov_b64 s[2:3], s[48:49]
	v_pk_mul_f32 v[72:73], v[198:199], s[54:55] op_sel_hi:[1,0]
	v_pk_mul_f32 v[70:71], v[196:197], s[54:55] op_sel_hi:[1,0]
	v_pk_mul_f32 v[68:69], v[200:201], s[54:55] op_sel_hi:[1,0]
	v_pk_mul_f32 v[76:77], v[60:61], v[70:71]
	v_mov_b32_e32 v60, v133
	v_cvt_pk_fp8_f32 v60, v76, v77
	v_pk_mul_f32 v[62:63], v[62:63], v[72:73]
	v_pk_mul_f32 v[48:49], v[48:49], v[68:69]
	v_pk_mul_f32 v[46:47], v[46:47], v[72:73]
	v_cvt_pk_fp8_f32 v60, v62, v63 op_sel:[0,0,1]
	v_mov_b32_e32 v63, v133
	v_cvt_pk_fp8_f32 v63, v48, v49
	v_pk_mul_f32 v[48:49], v[44:45], v[70:71]
	v_mov_b32_e32 v44, v133
	v_cvt_pk_fp8_f32 v44, v48, v49
	v_pk_mul_f32 v[32:33], v[32:33], v[68:69]
	v_pk_mul_f32 v[30:31], v[30:31], v[72:73]
	v_pk_mul_f32 v[16:17], v[16:17], v[68:69]
	v_cvt_pk_fp8_f32 v44, v46, v47 op_sel:[0,0,1]
	v_mov_b32_e32 v47, v133
	v_cvt_pk_fp8_f32 v47, v32, v33
	v_pk_mul_f32 v[32:33], v[28:29], v[70:71]
	v_mov_b32_e32 v28, v133
	v_cvt_pk_fp8_f32 v28, v32, v33
	v_pk_mul_f32 v[56:57], v[56:57], v[68:69]
	v_mov_b32_e32 v61, v133
	v_pk_mul_f32 v[52:53], v[52:53], v[70:71]
	v_cvt_pk_fp8_f32 v28, v30, v31 op_sel:[0,0,1]
	v_mov_b32_e32 v31, v133
	v_cvt_pk_fp8_f32 v31, v16, v17
	v_pk_mul_f32 v[16:17], v[12:13], v[70:71]
	v_mov_b32_e32 v12, v133
	v_cvt_pk_fp8_f32 v12, v16, v17
	v_mov_b32_e32 v62, v133
	v_pk_mul_f32 v[24:25], v[24:25], v[68:69]
	v_mov_b32_e32 v29, v133
	v_pk_mul_f32 v[20:21], v[20:21], v[70:71]
	v_mov_b32_e32 v30, v133
	v_pk_mul_f32 v[14:15], v[14:15], v[72:73]
	v_cvt_pk_fp8_f32 v61, v56, v57
	v_cvt_pk_fp8_f32 v62, v52, v53
	v_pk_mul_f32 v[40:41], v[40:41], v[68:69]
	v_mov_b32_e32 v45, v133
	v_pk_mul_f32 v[36:37], v[36:37], v[70:71]
	v_mov_b32_e32 v46, v133
	v_cvt_pk_fp8_f32 v29, v24, v25
	v_cvt_pk_fp8_f32 v30, v20, v21
	v_cvt_pk_fp8_f32 v12, v14, v15 op_sel:[0,0,1]
	v_pk_mul_f32 v[8:9], v[8:9], v[68:69]
	v_mov_b32_e32 v13, v133
	v_pk_mul_f32 v[4:5], v[4:5], v[70:71]
	v_mov_b32_e32 v14, v133
	v_pk_mul_f32 v[0:1], v[0:1], v[68:69]
	v_mov_b32_e32 v15, v133
	v_cvt_pk_fp8_f32 v45, v40, v41
	v_cvt_pk_fp8_f32 v46, v36, v37
	v_cvt_pk_fp8_f32 v13, v8, v9
	v_cvt_pk_fp8_f32 v14, v4, v5
	v_cvt_pk_fp8_f32 v15, v0, v1
	v_pk_mul_f32 v[74:75], v[202:203], s[54:55] op_sel_hi:[1,0]
	v_pk_mul_f32 v[54:55], v[54:55], v[72:73]
	v_pk_mul_f32 v[58:59], v[58:59], v[74:75]
	v_pk_mul_f32 v[50:51], v[50:51], v[74:75]
	v_pk_mul_f32 v[26:27], v[26:27], v[74:75]
	v_pk_mul_f32 v[22:23], v[22:23], v[72:73]
	v_pk_mul_f32 v[18:19], v[18:19], v[74:75]
	v_cvt_pk_fp8_f32 v61, v58, v59 op_sel:[0,0,1]
	v_cvt_pk_fp8_f32 v62, v54, v55 op_sel:[0,0,1]
	v_cvt_pk_fp8_f32 v63, v50, v51 op_sel:[0,0,1]
	v_pk_mul_f32 v[42:43], v[42:43], v[74:75]
	v_pk_mul_f32 v[38:39], v[38:39], v[72:73]
	v_pk_mul_f32 v[34:35], v[34:35], v[74:75]
	v_cvt_pk_fp8_f32 v29, v26, v27 op_sel:[0,0,1]
	v_cvt_pk_fp8_f32 v30, v22, v23 op_sel:[0,0,1]
	v_cvt_pk_fp8_f32 v31, v18, v19 op_sel:[0,0,1]
	v_pk_mul_f32 v[10:11], v[10:11], v[74:75]
	v_pk_mul_f32 v[6:7], v[6:7], v[72:73]
	v_pk_mul_f32 v[2:3], v[2:3], v[74:75]
	v_cvt_pk_fp8_f32 v45, v42, v43 op_sel:[0,0,1]
	v_cvt_pk_fp8_f32 v46, v38, v39 op_sel:[0,0,1]
	v_cvt_pk_fp8_f32 v47, v34, v35 op_sel:[0,0,1]
	v_cvt_pk_fp8_f32 v13, v10, v11 op_sel:[0,0,1]
	v_cvt_pk_fp8_f32 v14, v6, v7 op_sel:[0,0,1]
	v_cvt_pk_fp8_f32 v15, v2, v3 op_sel:[0,0,1]
	v_permlane32_swap_b32_e32 v60, v62
	v_permlane32_swap_b32_e32 v61, v63
	v_permlane32_swap_b32_e32 v28, v30
	v_permlane32_swap_b32_e32 v29, v31
	v_permlane16_swap_b32_e32 v60, v61
	v_permlane16_swap_b32_e32 v62, v63
	v_permlane32_swap_b32_e32 v44, v46
	v_permlane32_swap_b32_e32 v45, v47
	v_permlane16_swap_b32_e32 v28, v29
	v_permlane16_swap_b32_e32 v30, v31
	v_permlane32_swap_b32_e32 v12, v14
	v_permlane32_swap_b32_e32 v13, v15
	v_permlane16_swap_b32_e32 v44, v45
	v_permlane16_swap_b32_e32 v46, v47
	global_store_dwordx4 v[128:129], v[60:63], off offset:128
	global_store_dwordx4 v[96:97], v[44:47], off offset:128
	v_permlane16_swap_b32_e32 v12, v13
	v_permlane16_swap_b32_e32 v14, v15
	global_store_dwordx4 v[64:65], v[28:31], off offset:128
	global_store_dwordx4 v[66:67], v[12:15], off offset:128
	s_cbranch_vccz .LBB0_1496
	v_readlane_b32 s0, v252, 18
	s_waitcnt vmcnt(0)
	v_readlane_b32 s1, v252, 19
	s_andn2_b64 vcc, exec, s[0:1]
	s_cbranch_vccnz .LBB0_1227
	s_barrier
	s_branch .LBB0_1227

.Lpeel_exit_7:
	s_ashr_i32 s11, s18, 4
	s_mul_hi_i32 s13, s11, 0xc000
	s_mul_i32 s11, s11, 0xc000
	s_add_u32 s11, s37, s11
	s_addc_u32 s13, s38, s13
	s_lshl_b32 s20, s49, 8
	s_ashr_i32 s21, s20, 31
	s_lshl_b64 s[22:23], s[20:21], 2
	s_add_u32 s11, s11, s22
	v_mbcnt_lo_u32_b32 v134, -1, 0
	v_mbcnt_hi_u32_b32 v134, -1, v134
	s_addc_u32 s13, s13, s23
	v_ashrrev_i32_e32 v135, 4, v134
	s_add_u32 s22, s11, s46
	v_lshlrev_b32_e32 v132, 2, v135
	s_addc_u32 s23, s13, 0
	v_ashrrev_i32_e32 v133, 31, v132
	v_lshl_add_u64 v[132:133], v[132:133], 2, s[22:23]
	global_load_dwordx4 v[146:149], v[132:133], off
	global_load_dwordx4 v[150:153], v[132:133], off offset:64
	global_load_dwordx4 v[196:199], v[132:133], off offset:512
	global_load_dwordx4 v[200:203], v[132:133], off offset:576
	v_mov_b32_e32 v164, v129
	s_lshl_b32 s11, s18, 8
	v_mov_b32_e32 v165, v129
	s_add_i32 s22, s11, s39
	s_ashr_i32 s23, s22, 31
	s_lshl_b64 s[22:23], s[22:23], 11
	s_add_u32 s11, s35, s22
	s_addc_u32 s13, s36, s23
	v_mov_b32_e32 v162, v129
	v_lshlrev_b32_e32 v135, 3, v135
	s_add_u32 s11, s11, s20
	v_mov_b32_e32 v154, v129
	v_mov_b32_e32 v155, v129
	v_mov_b32_e32 v156, v129
	v_mov_b32_e32 v157, v129
	v_and_b32_e32 v128, 16, v134
	v_bfi_b32 v134, -16, v135, v134
	s_addc_u32 s13, s13, s21
	v_mov_b32_e32 v163, v129
	v_mov_b32_e32 v158, v129
	v_mov_b32_e32 v159, v129
	v_mov_b32_e32 v160, v129
	v_mov_b32_e32 v161, v129
	v_ashrrev_i32_e32 v135, 31, v134
	s_add_u32 s20, s11, s40
	v_lshlrev_b64 v[134:135], 11, v[134:135]
	s_addc_u32 s21, s13, 0
	v_lshl_add_u64 v[134:135], s[20:21], 0, v[134:135]
	v_lshl_add_u64 v[134:135], v[134:135], 0, v[128:129]
	v_add_co_u32_e32 v136, vcc, s34, v134
	s_mov_b32 s18, s12
	s_nop 0
	v_addc_co_u32_e32 v137, vcc, 0, v135, vcc
	s_mov_b32 s49, s10
	s_mov_b64 s[22:23], s[16:17]
	s_mov_b64 s[20:21], s[14:15]
	s_waitcnt vmcnt(0)
	v_pk_mul_f32 v[146:147], v[146:147], s[8:9] op_sel_hi:[1,0]
	v_pk_mul_f32 v[150:151], v[150:151], s[8:9] op_sel_hi:[1,0]
	v_pk_mul_f32 v[84:85], v[84:85], v[146:147]
	v_pk_mul_f32 v[80:81], v[80:81], v[150:151]
	v_cvt_pk_fp8_f32 v164, v84, v85
	v_cvt_pk_fp8_f32 v165, v80, v81
	v_pk_mul_f32 v[148:149], v[148:149], s[8:9] op_sel_hi:[1,0]
	v_pk_mul_f32 v[152:153], v[152:153], s[8:9] op_sel_hi:[1,0]
	v_pk_mul_f32 v[80:81], v[86:87], v[148:149]
	v_pk_mul_f32 v[72:73], v[72:73], v[150:151]
	v_cvt_pk_fp8_f32 v164, v80, v81 op_sel:[0,0,1]
	v_pk_mul_f32 v[80:81], v[82:83], v[152:153]
	v_pk_mul_f32 v[92:93], v[92:93], v[146:147]
	v_cvt_pk_fp8_f32 v165, v80, v81 op_sel:[0,0,1]
	v_pk_mul_f32 v[80:81], v[76:77], v[146:147]
	v_mov_b32_e32 v77, v129
	v_mov_b32_e32 v76, v129
	v_cvt_pk_fp8_f32 v77, v72, v73
	v_pk_mul_f32 v[72:73], v[78:79], v[148:149]
	v_pk_mul_f32 v[68:69], v[68:69], v[146:147]
	v_mov_b32_e32 v78, v129
	v_pk_mul_f32 v[124:125], v[124:125], v[146:147]
	v_pk_mul_f32 v[120:121], v[120:121], v[150:151]
	v_pk_mul_f32 v[116:117], v[116:117], v[146:147]
	v_pk_mul_f32 v[112:113], v[112:113], v[150:151]
	v_cvt_pk_fp8_f32 v162, v92, v93
	v_pk_mul_f32 v[88:89], v[88:89], v[150:151]
	v_cvt_pk_fp8_f32 v76, v80, v81
	v_cvt_pk_fp8_f32 v78, v68, v69
	v_pk_mul_f32 v[64:65], v[64:65], v[150:151]
	v_mov_b32_e32 v79, v129
	v_pk_mul_f32 v[108:109], v[108:109], v[146:147]
	v_pk_mul_f32 v[104:105], v[104:105], v[150:151]
	v_pk_mul_f32 v[100:101], v[100:101], v[146:147]
	v_pk_mul_f32 v[96:97], v[96:97], v[150:151]
	v_cvt_pk_fp8_f32 v154, v124, v125
	v_cvt_pk_fp8_f32 v155, v120, v121
	v_cvt_pk_fp8_f32 v156, v116, v117
	v_cvt_pk_fp8_f32 v157, v112, v113
	v_cvt_pk_fp8_f32 v163, v88, v89
	v_cvt_pk_fp8_f32 v79, v64, v65
	v_cvt_pk_fp8_f32 v158, v108, v109
	v_cvt_pk_fp8_f32 v159, v104, v105
	v_cvt_pk_fp8_f32 v160, v100, v101
	v_cvt_pk_fp8_f32 v161, v96, v97
	v_pk_mul_f32 v[88:89], v[94:95], v[148:149]
	v_pk_mul_f32 v[64:65], v[70:71], v[148:149]
	v_pk_mul_f32 v[126:127], v[126:127], v[148:149]
	v_pk_mul_f32 v[122:123], v[122:123], v[152:153]
	v_pk_mul_f32 v[118:119], v[118:119], v[148:149]
	v_pk_mul_f32 v[114:115], v[114:115], v[152:153]
	v_cvt_pk_fp8_f32 v162, v88, v89 op_sel:[0,0,1]
	v_pk_mul_f32 v[88:89], v[90:91], v[152:153]
	v_cvt_pk_fp8_f32 v76, v72, v73 op_sel:[0,0,1]
	v_pk_mul_f32 v[72:73], v[74:75], v[152:153]
	v_cvt_pk_fp8_f32 v78, v64, v65 op_sel:[0,0,1]
	v_pk_mul_f32 v[64:65], v[66:67], v[152:153]
	v_pk_mul_f32 v[110:111], v[110:111], v[148:149]
	v_pk_mul_f32 v[106:107], v[106:107], v[152:153]
	v_pk_mul_f32 v[102:103], v[102:103], v[148:149]
	v_pk_mul_f32 v[98:99], v[98:99], v[152:153]
	v_cvt_pk_fp8_f32 v154, v126, v127 op_sel:[0,0,1]
	v_cvt_pk_fp8_f32 v155, v122, v123 op_sel:[0,0,1]
	v_cvt_pk_fp8_f32 v156, v118, v119 op_sel:[0,0,1]
	v_cvt_pk_fp8_f32 v157, v114, v115 op_sel:[0,0,1]
	v_cvt_pk_fp8_f32 v163, v88, v89 op_sel:[0,0,1]
	v_cvt_pk_fp8_f32 v77, v72, v73 op_sel:[0,0,1]
	v_cvt_pk_fp8_f32 v79, v64, v65 op_sel:[0,0,1]
	v_cvt_pk_fp8_f32 v158, v110, v111 op_sel:[0,0,1]
	v_cvt_pk_fp8_f32 v159, v106, v107 op_sel:[0,0,1]
	v_cvt_pk_fp8_f32 v160, v102, v103 op_sel:[0,0,1]
	v_cvt_pk_fp8_f32 v161, v98, v99 op_sel:[0,0,1]
	v_add_co_u32_e32 v80, vcc, s47, v134
	v_permlane32_swap_b32_e32 v154, v156
	s_nop 0
	v_addc_co_u32_e32 v81, vcc, 0, v135, vcc
	v_permlane32_swap_b32_e32 v155, v157
	v_permlane32_swap_b32_e32 v162, v164
	v_permlane32_swap_b32_e32 v163, v165
	v_permlane32_swap_b32_e32 v76, v78
	v_permlane32_swap_b32_e32 v77, v79
	v_add_co_u32_e32 v82, vcc, s48, v134
	v_permlane32_swap_b32_e32 v158, v160
	v_permlane32_swap_b32_e32 v159, v161
	v_permlane16_swap_b32_e32 v154, v155
	v_permlane16_swap_b32_e32 v156, v157
	v_permlane16_swap_b32_e32 v162, v163
	v_permlane16_swap_b32_e32 v164, v165
	v_permlane16_swap_b32_e32 v76, v77
	v_permlane16_swap_b32_e32 v78, v79
	v_addc_co_u32_e32 v83, vcc, 0, v135, vcc
	v_permlane16_swap_b32_e32 v158, v159
	v_permlane16_swap_b32_e32 v160, v161
	global_store_dwordx4 v[134:135], v[154:157], off
	global_store_dwordx4 v[136:137], v[158:161], off
	global_store_dwordx4 v[80:81], v[162:165], off
	global_store_dwordx4 v[82:83], v[76:79], off
	v_mov_b32_e32 v75, v129
	v_mov_b32_e32 v72, v129
	v_mov_b32_e32 v73, v129
	v_mov_b32_e32 v74, v129
	s_and_b64 vcc, exec, s[4:5]
	v_pk_mul_f32 v[64:65], v[196:197], s[8:9] op_sel_hi:[1,0]
	v_pk_mul_f32 v[68:69], v[200:201], s[8:9] op_sel_hi:[1,0]
	v_pk_mul_f32 v[70:71], v[202:203], s[8:9] op_sel_hi:[1,0]
	v_pk_mul_f32 v[48:49], v[48:49], v[68:69]
	v_pk_mul_f32 v[66:67], v[198:199], s[8:9] op_sel_hi:[1,0]
	v_cvt_pk_fp8_f32 v75, v48, v49
	v_pk_mul_f32 v[48:49], v[50:51], v[70:71]
	v_pk_mul_f32 v[40:41], v[40:41], v[68:69]
	v_pk_mul_f32 v[36:37], v[36:37], v[64:65]
	v_cvt_pk_fp8_f32 v75, v48, v49 op_sel:[0,0,1]
	v_pk_mul_f32 v[48:49], v[44:45], v[64:65]
	v_mov_b32_e32 v45, v129
	v_cvt_pk_fp8_f32 v45, v40, v41
	v_pk_mul_f32 v[40:41], v[46:47], v[66:67]
	v_mov_b32_e32 v46, v129
	v_cvt_pk_fp8_f32 v46, v36, v37
	v_pk_mul_f32 v[32:33], v[32:33], v[68:69]
	v_mov_b32_e32 v47, v129
	v_cvt_pk_fp8_f32 v47, v32, v33
	v_pk_mul_f32 v[32:33], v[38:39], v[66:67]
	v_pk_mul_f32 v[24:25], v[24:25], v[68:69]
	v_cvt_pk_fp8_f32 v46, v32, v33 op_sel:[0,0,1]
	v_pk_mul_f32 v[32:33], v[34:35], v[70:71]
	v_pk_mul_f32 v[20:21], v[20:21], v[64:65]
	v_cvt_pk_fp8_f32 v47, v32, v33 op_sel:[0,0,1]
	v_pk_mul_f32 v[32:33], v[28:29], v[64:65]
	v_mov_b32_e32 v29, v129
	v_cvt_pk_fp8_f32 v29, v24, v25
	v_pk_mul_f32 v[24:25], v[30:31], v[66:67]
	v_mov_b32_e32 v30, v129
	v_cvt_pk_fp8_f32 v30, v20, v21
	v_pk_mul_f32 v[16:17], v[16:17], v[68:69]
	v_mov_b32_e32 v31, v129
	v_cvt_pk_fp8_f32 v31, v16, v17
	v_pk_mul_f32 v[16:17], v[22:23], v[66:67]
	v_mov_b32_e32 v28, v129
	v_cvt_pk_fp8_f32 v30, v16, v17 op_sel:[0,0,1]
	v_pk_mul_f32 v[16:17], v[18:19], v[70:71]
	v_pk_mul_f32 v[8:9], v[8:9], v[68:69]
	v_cvt_pk_fp8_f32 v31, v16, v17 op_sel:[0,0,1]
	v_pk_mul_f32 v[16:17], v[12:13], v[64:65]
	v_mov_b32_e32 v13, v129
	v_pk_mul_f32 v[60:61], v[60:61], v[64:65]
	v_pk_mul_f32 v[56:57], v[56:57], v[68:69]
	v_pk_mul_f32 v[52:53], v[52:53], v[64:65]
	v_mov_b32_e32 v44, v129
	v_cvt_pk_fp8_f32 v28, v32, v33
	v_mov_b32_e32 v12, v129
	v_cvt_pk_fp8_f32 v13, v8, v9
	v_pk_mul_f32 v[8:9], v[14:15], v[66:67]
	v_pk_mul_f32 v[4:5], v[4:5], v[64:65]
	v_mov_b32_e32 v14, v129
	v_cvt_pk_fp8_f32 v72, v60, v61
	v_cvt_pk_fp8_f32 v73, v56, v57
	v_cvt_pk_fp8_f32 v74, v52, v53
	v_cvt_pk_fp8_f32 v44, v48, v49
	v_cvt_pk_fp8_f32 v12, v16, v17
	v_cvt_pk_fp8_f32 v14, v4, v5
	v_pk_mul_f32 v[0:1], v[0:1], v[68:69]
	v_mov_b32_e32 v15, v129
	v_cvt_pk_fp8_f32 v15, v0, v1
	v_pk_mul_f32 v[62:63], v[62:63], v[66:67]
	v_pk_mul_f32 v[58:59], v[58:59], v[70:71]
	v_pk_mul_f32 v[54:55], v[54:55], v[66:67]
	v_cvt_pk_fp8_f32 v28, v24, v25 op_sel:[0,0,1]
	v_pk_mul_f32 v[24:25], v[26:27], v[70:71]
	v_pk_mul_f32 v[0:1], v[6:7], v[66:67]
	v_cvt_pk_fp8_f32 v72, v62, v63 op_sel:[0,0,1]
	v_cvt_pk_fp8_f32 v73, v58, v59 op_sel:[0,0,1]
	v_cvt_pk_fp8_f32 v74, v54, v55 op_sel:[0,0,1]
	v_cvt_pk_fp8_f32 v44, v40, v41 op_sel:[0,0,1]
	v_pk_mul_f32 v[40:41], v[42:43], v[70:71]
	v_cvt_pk_fp8_f32 v29, v24, v25 op_sel:[0,0,1]
	v_cvt_pk_fp8_f32 v12, v8, v9 op_sel:[0,0,1]
	v_pk_mul_f32 v[8:9], v[10:11], v[70:71]
	v_cvt_pk_fp8_f32 v14, v0, v1 op_sel:[0,0,1]
	v_pk_mul_f32 v[0:1], v[2:3], v[70:71]
	v_cvt_pk_fp8_f32 v45, v40, v41 op_sel:[0,0,1]
	v_cvt_pk_fp8_f32 v13, v8, v9 op_sel:[0,0,1]
	v_cvt_pk_fp8_f32 v15, v0, v1 op_sel:[0,0,1]
	v_permlane32_swap_b32_e32 v72, v74
	v_permlane32_swap_b32_e32 v73, v75
	v_permlane32_swap_b32_e32 v28, v30
	v_permlane32_swap_b32_e32 v29, v31
	v_permlane16_swap_b32_e32 v72, v73
	v_permlane16_swap_b32_e32 v74, v75
	v_permlane32_swap_b32_e32 v44, v46
	v_permlane32_swap_b32_e32 v45, v47
	v_permlane16_swap_b32_e32 v28, v29
	v_permlane16_swap_b32_e32 v30, v31
	v_permlane32_swap_b32_e32 v12, v14
	v_permlane32_swap_b32_e32 v13, v15
	v_permlane16_swap_b32_e32 v44, v45
	v_permlane16_swap_b32_e32 v46, v47
	global_store_dwordx4 v[134:135], v[72:75], off offset:128
	global_store_dwordx4 v[136:137], v[44:47], off offset:128
	v_permlane16_swap_b32_e32 v12, v13
	v_permlane16_swap_b32_e32 v14, v15
	global_store_dwordx4 v[80:81], v[28:31], off offset:128
	global_store_dwordx4 v[82:83], v[12:15], off offset:128
	s_cbranch_vccz .LBB0_4925
	s_waitcnt vmcnt(0)
	v_readlane_b32 s0, v252, 2
	s_cmpk_gt_u32 s0, 0xff
	s_cbranch_scc1 .LBB0_4936
	s_barrier
